# barrier L1 invalidate issued right after the arrive atomic (and first poll) with counted vmcnt waits, so the last arriver does not wait for it before proceeding
# baseline (speedup 1.0000x reference)
; __device__ __forceinline__ unsigned xb_ld(unsigned* p)              { return __hip_atomic_load(p, __ATOMIC_RELAXED, __HIP_MEMORY_SCOPE_AGENT); }
; __device__ __forceinline__ unsigned xb_add(unsigned* p, unsigned v) { return __hip_atomic_fetch_add(p, v, __ATOMIC_RELAXED, __HIP_MEMORY_SCOPE_AGENT); }
; #define XB_SPIN(cond, bar) do { unsigned _sp = 0; while (cond) { __builtin_amdgcn_s_sleep(1); \
;     if ((++_sp & 255u) == 0u) { if (xb_ld(&(bar)[XB_TMO])) break; if (_sp > XB_SPIN_CAP) { atomicAdd(&(bar)[XB_TMO], 1u); break; } } } } while (0)
; __device__ __forceinline__ void xcd_barrier(const XcdBarrier& b, const bool xb_leader) {
;     ...
;         const unsigned old = xb_add(&bar[XB_XSUB(b.x)], 1u);
;         const unsigned gen = old / nloc;
;         if (old + 1u == (gen + 1u) * nloc) {
;             __builtin_amdgcn_fence(__ATOMIC_RELEASE, "agent");
;             asm volatile("s_waitcnt vmcnt(0)" ::: "memory");
;             const unsigned og = xb_add(&bar[XB_TOP], 1u);
;             const unsigned tg = og / nx;
;             if (og + 1u == (tg + 1u) * nx) xb_add(&bar[XB_TOPGEN], 1u);
;             else XB_SPIN(xb_ld(&bar[XB_TOPGEN]) == tg, bar);
;             __builtin_amdgcn_fence(__ATOMIC_ACQUIRE, "agent");
;             xb_add(&bar[XB_XGEN(b.x)], 1u);
;             asm volatile("s_waitcnt vmcnt(0)" ::: "memory");
;         } else {
;             XB_SPIN(xb_ld(&bar[XB_XGEN(b.x)]) == gen, bar);
.LBB0_85:
	s_mov_b64 s[6:7], exec
	v_readlane_b32 s3, v254, 21
	s_lshl_b32 s3, s3, 8
	v_mbcnt_lo_u32_b32 v0, s6, 0
	s_add_u32 s4, s28, s3
	v_mbcnt_hi_u32_b32 v0, s7, v0
	s_addc_u32 s5, s29, 0
	v_cmp_eq_u32_e32 vcc, 0, v0
	s_and_saveexec_b64 s[12:13], vcc
	s_cbranch_execz .LBB0_87
	s_bcnt1_i32_b64 s3, s[6:7]
	v_mov_b32_e32 v1, 0x1000
	v_mov_b32_e32 v2, s3
	global_atomic_add v1, v1, v2, s[4:5] offset:1024 sc0
	buffer_inv sc1
.LBB0_87:
	s_or_b64 exec, exec, s[12:13]
	v_cvt_f32_u32_e32 v2, v9
	s_waitcnt vmcnt(1)
	v_readfirstlane_b32 s3, v1
	v_sub_u32_e32 v1, 0, v9
	v_rcp_iflag_f32_e32 v2, v2
	v_add_u32_e32 v3, s3, v0
	v_mul_f32_e32 v2, 0x4f7ffffe, v2
	v_cvt_u32_f32_e32 v2, v2
	v_mul_lo_u32 v0, v1, v2
	v_mul_hi_u32 v0, v2, v0
	v_add_u32_e32 v0, v2, v0
	v_mul_hi_u32 v0, v3, v0
	v_mul_lo_u32 v1, v0, v9
	v_sub_u32_e32 v1, v3, v1
	v_add_u32_e32 v2, 1, v0
	v_cmp_ge_u32_e32 vcc, v1, v9
	s_nop 1
	v_cndmask_b32_e32 v0, v0, v2, vcc
	v_sub_u32_e32 v2, v1, v9
	v_cndmask_b32_e32 v1, v1, v2, vcc
	v_add_u32_e32 v2, 1, v0
	v_cmp_ge_u32_e32 vcc, v1, v9
	v_add_u32_e32 v1, 1, v3
	s_nop 0
	v_cndmask_b32_e32 v0, v0, v2, vcc
	v_mul_lo_u32 v2, v9, v0
	v_add_u32_e32 v2, v2, v9
	v_cmp_ne_u32_e32 vcc, v1, v2
	s_and_saveexec_b64 s[6:7], vcc
	s_xor_b64 s[6:7], exec, s[6:7]
	s_cbranch_execz .LBB0_101
	v_mov_b32_e32 v1, 0x3100
	global_load_dword v1, v1, s[28:29] offset:1024 sc1
	s_add_u32 s14, s28, 0x3500
	s_addc_u32 s15, s29, 0
	s_waitcnt vmcnt(0)
	v_cmp_eq_u32_e32 vcc, v1, v0
	s_and_saveexec_b64 s[12:13], vcc
	s_cbranch_execz .LBB0_100
	s_mov_b32 s3, 1
	s_mov_b64 s[16:17], 0
	v_mov_b32_e32 v1, 0
	s_branch .LBB0_91

; __device__ __forceinline__ unsigned xb_ld(unsigned* p)              { return __hip_atomic_load(p, __ATOMIC_RELAXED, __HIP_MEMORY_SCOPE_AGENT); }
; __device__ __forceinline__ unsigned xb_add(unsigned* p, unsigned v) { return __hip_atomic_fetch_add(p, v, __ATOMIC_RELAXED, __HIP_MEMORY_SCOPE_AGENT); }
; #define XB_SPIN(cond, bar) do { unsigned _sp = 0; while (cond) { __builtin_amdgcn_s_sleep(1); \
;     if ((++_sp & 255u) == 0u) { if (xb_ld(&(bar)[XB_TMO])) break; if (_sp > XB_SPIN_CAP) { atomicAdd(&(bar)[XB_TMO], 1u); break; } } } } while (0)
; __device__ __forceinline__ void xcc_barrier(unsigned* bar, unsigned* cnt, unsigned nloc, const bool xb_leader) {
;     ...
;         __builtin_amdgcn_s_waitcnt(0);
;         const unsigned old = xb_add(cnt, 1u), target = (old / nloc + 1u) * nloc;
;         XB_SPIN(xb_ld(cnt) < target, bar);
.LBB0_137:
	s_or_b64 exec, exec, s[10:11]
	v_mov_b32_e32 v0, 0
	global_load_dword v3, v0, s[6:7] sc1
	buffer_inv sc1
	s_ashr_i32 s3, s33, 31
	s_lshr_b32 s3, s3, 29
	s_add_i32 s3, s33, s3
	s_ashr_i32 s8, s3, 3
	v_cvt_f32_u32_e32 v4, s8
	s_sub_i32 s3, 0, s8
	s_waitcnt vmcnt(2)
	v_readfirstlane_b32 s9, v2
	v_rcp_iflag_f32_e32 v4, v4
	s_nop 0
	v_add_u32_e32 v1, s9, v1
	v_mul_f32_e32 v4, 0x4f7ffffe, v4
	v_cvt_u32_f32_e32 v4, v4
	v_mul_lo_u32 v2, s3, v4
	v_mul_hi_u32 v2, v4, v2
	v_add_u32_e32 v2, v4, v2
	v_mul_hi_u32 v2, v1, v2
	v_mul_lo_u32 v4, v2, s8
	v_sub_u32_e32 v1, v1, v4
	v_add_u32_e32 v4, 1, v2
	v_cmp_le_u32_e32 vcc, s8, v1
	s_mov_b32 s3, 1
	s_nop 0
	v_cndmask_b32_e32 v2, v2, v4, vcc
	v_subrev_u32_e32 v4, s8, v1
	v_cndmask_b32_e32 v1, v1, v4, vcc
	v_add_u32_e32 v4, 1, v2
	v_cmp_le_u32_e32 vcc, s8, v1
	s_nop 1
	v_cndmask_b32_e32 v1, v2, v4, vcc
	v_mul_lo_u32 v1, s8, v1
	v_add_u32_e32 v1, s8, v1
	s_waitcnt vmcnt(1)
	v_cmp_lt_u32_e32 vcc, v3, v1
	s_and_saveexec_b64 s[8:9], vcc
	s_cbranch_execz .LBB0_149
	s_mov_b64 s[10:11], 0
	s_branch .LBB0_140

; __device__ __forceinline__ unsigned xb_ld(unsigned* p)              { return __hip_atomic_load(p, __ATOMIC_RELAXED, __HIP_MEMORY_SCOPE_AGENT); }
; __device__ __forceinline__ unsigned xb_add(unsigned* p, unsigned v) { return __hip_atomic_fetch_add(p, v, __ATOMIC_RELAXED, __HIP_MEMORY_SCOPE_AGENT); }
; #define XB_SPIN(cond, bar) do { unsigned _sp = 0; while (cond) { __builtin_amdgcn_s_sleep(1); \
;     if ((++_sp & 255u) == 0u) { if (xb_ld(&(bar)[XB_TMO])) break; if (_sp > XB_SPIN_CAP) { atomicAdd(&(bar)[XB_TMO], 1u); break; } } } } while (0)
; __device__ __forceinline__ void xcd_barrier(const XcdBarrier& b, const bool xb_leader) {
;     ...
;         const unsigned old = xb_add(&bar[XB_XSUB(b.x)], 1u);
;         const unsigned gen = old / nloc;
;         if (old + 1u == (gen + 1u) * nloc) {
;             __builtin_amdgcn_fence(__ATOMIC_RELEASE, "agent");
;             asm volatile("s_waitcnt vmcnt(0)" ::: "memory");
;             const unsigned og = xb_add(&bar[XB_TOP], 1u);
;             const unsigned tg = og / nx;
;             if (og + 1u == (tg + 1u) * nx) xb_add(&bar[XB_TOPGEN], 1u);
;             else XB_SPIN(xb_ld(&bar[XB_TOPGEN]) == tg, bar);
;             __builtin_amdgcn_fence(__ATOMIC_ACQUIRE, "agent");
;             xb_add(&bar[XB_XGEN(b.x)], 1u);
;             asm volatile("s_waitcnt vmcnt(0)" ::: "memory");
;         } else {
;             XB_SPIN(xb_ld(&bar[XB_XGEN(b.x)]) == gen, bar);
.LBB0_178:
	s_mov_b64 s[8:9], exec
	v_readlane_b32 s3, v254, 21
	s_lshl_b32 s3, s3, 8
	v_mbcnt_lo_u32_b32 v0, s8, 0
	s_add_u32 s6, s28, s3
	v_mbcnt_hi_u32_b32 v0, s9, v0
	s_addc_u32 s7, s29, 0
	v_cmp_eq_u32_e32 vcc, 0, v0
	s_and_saveexec_b64 s[10:11], vcc
	s_cbranch_execz .LBB0_180
	s_bcnt1_i32_b64 s3, s[8:9]
	v_mov_b32_e32 v1, 0x1000
	v_mov_b32_e32 v2, s3
	global_atomic_add v1, v1, v2, s[6:7] offset:1024 sc0
	buffer_inv sc1
.LBB0_180:
	s_or_b64 exec, exec, s[10:11]
	v_cvt_f32_u32_e32 v2, v9
	s_waitcnt vmcnt(1)
	v_readfirstlane_b32 s3, v1
	v_sub_u32_e32 v1, 0, v9
	v_rcp_iflag_f32_e32 v2, v2
	v_add_u32_e32 v3, s3, v0
	v_mul_f32_e32 v2, 0x4f7ffffe, v2
	v_cvt_u32_f32_e32 v2, v2
	v_mul_lo_u32 v0, v1, v2
	v_mul_hi_u32 v0, v2, v0
	v_add_u32_e32 v0, v2, v0
	v_mul_hi_u32 v0, v3, v0
	v_mul_lo_u32 v1, v0, v9
	v_sub_u32_e32 v1, v3, v1
	v_add_u32_e32 v2, 1, v0
	v_cmp_ge_u32_e32 vcc, v1, v9
	s_nop 1
	v_cndmask_b32_e32 v0, v0, v2, vcc
	v_sub_u32_e32 v2, v1, v9
	v_cndmask_b32_e32 v1, v1, v2, vcc
	v_add_u32_e32 v2, 1, v0
	v_cmp_ge_u32_e32 vcc, v1, v9
	v_add_u32_e32 v1, 1, v3
	s_nop 0
	v_cndmask_b32_e32 v0, v0, v2, vcc
	v_mul_lo_u32 v2, v9, v0
	v_add_u32_e32 v2, v2, v9
	v_cmp_ne_u32_e32 vcc, v1, v2
	s_and_saveexec_b64 s[8:9], vcc
	s_xor_b64 s[8:9], exec, s[8:9]
	s_cbranch_execz .LBB0_194
	v_mov_b32_e32 v1, 0x3100
	global_load_dword v1, v1, s[28:29] offset:1024 sc1
	s_add_u32 s12, s28, 0x3500
	s_addc_u32 s13, s29, 0
	s_waitcnt vmcnt(0)
	v_cmp_eq_u32_e32 vcc, v1, v0
	s_and_saveexec_b64 s[10:11], vcc
	s_cbranch_execz .LBB0_193
	s_mov_b32 s3, 1
	s_mov_b64 s[14:15], 0
	v_mov_b32_e32 v1, 0
	s_branch .LBB0_184

; __device__ __forceinline__ unsigned xb_ld(unsigned* p)              { return __hip_atomic_load(p, __ATOMIC_RELAXED, __HIP_MEMORY_SCOPE_AGENT); }
; __device__ __forceinline__ unsigned xb_add(unsigned* p, unsigned v) { return __hip_atomic_fetch_add(p, v, __ATOMIC_RELAXED, __HIP_MEMORY_SCOPE_AGENT); }
; #define XB_SPIN(cond, bar) do { unsigned _sp = 0; while (cond) { __builtin_amdgcn_s_sleep(1); \
;     if ((++_sp & 255u) == 0u) { if (xb_ld(&(bar)[XB_TMO])) break; if (_sp > XB_SPIN_CAP) { atomicAdd(&(bar)[XB_TMO], 1u); break; } } } } while (0)
; __device__ __forceinline__ void xcc_barrier(unsigned* bar, unsigned* cnt, unsigned nloc, const bool xb_leader) {
;     ...
;         __builtin_amdgcn_s_waitcnt(0);
;         const unsigned old = xb_add(cnt, 1u), target = (old / nloc + 1u) * nloc;
;         XB_SPIN(xb_ld(cnt) < target, bar);
.LBB0_748:
	s_or_b64 exec, exec, s[8:9]
	v_mov_b32_e32 v0, 0
	global_load_dword v3, v0, s[4:5] sc1
	buffer_inv sc1
	s_ashr_i32 s3, s33, 31
	s_lshr_b32 s3, s3, 29
	s_add_i32 s3, s33, s3
	s_ashr_i32 s6, s3, 3
	v_cvt_f32_u32_e32 v4, s6
	s_sub_i32 s3, 0, s6
	s_waitcnt vmcnt(2)
	v_readfirstlane_b32 s7, v2
	v_rcp_iflag_f32_e32 v4, v4
	s_nop 0
	v_add_u32_e32 v1, s7, v1
	v_mul_f32_e32 v4, 0x4f7ffffe, v4
	v_cvt_u32_f32_e32 v4, v4
	v_mul_lo_u32 v2, s3, v4
	v_mul_hi_u32 v2, v4, v2
	v_add_u32_e32 v2, v4, v2
	v_mul_hi_u32 v2, v1, v2
	v_mul_lo_u32 v4, v2, s6
	v_sub_u32_e32 v1, v1, v4
	v_add_u32_e32 v4, 1, v2
	v_cmp_le_u32_e32 vcc, s6, v1
	s_mov_b32 s3, 1
	s_nop 0
	v_cndmask_b32_e32 v2, v2, v4, vcc
	v_subrev_u32_e32 v4, s6, v1
	v_cndmask_b32_e32 v1, v1, v4, vcc
	v_add_u32_e32 v4, 1, v2
	v_cmp_le_u32_e32 vcc, s6, v1
	s_nop 1
	v_cndmask_b32_e32 v1, v2, v4, vcc
	v_mul_lo_u32 v1, s6, v1
	v_add_u32_e32 v1, s6, v1
	s_waitcnt vmcnt(1)
	v_cmp_lt_u32_e32 vcc, v3, v1
	s_and_saveexec_b64 s[6:7], vcc
	s_cbranch_execz .LBB0_790
	s_mov_b64 s[8:9], 0
	s_branch .LBB0_751

; __device__ __forceinline__ unsigned xb_ld(unsigned* p)              { return __hip_atomic_load(p, __ATOMIC_RELAXED, __HIP_MEMORY_SCOPE_AGENT); }
; __device__ __forceinline__ unsigned xb_add(unsigned* p, unsigned v) { return __hip_atomic_fetch_add(p, v, __ATOMIC_RELAXED, __HIP_MEMORY_SCOPE_AGENT); }
; #define XB_SPIN(cond, bar) do { unsigned _sp = 0; while (cond) { __builtin_amdgcn_s_sleep(1); \
;     if ((++_sp & 255u) == 0u) { if (xb_ld(&(bar)[XB_TMO])) break; if (_sp > XB_SPIN_CAP) { atomicAdd(&(bar)[XB_TMO], 1u); break; } } } } while (0)
; __device__ __forceinline__ void xcd_barrier(const XcdBarrier& b, const bool xb_leader) {
;     ...
;         const unsigned old = xb_add(&bar[XB_XSUB(b.x)], 1u);
;         const unsigned gen = old / nloc;
;         if (old + 1u == (gen + 1u) * nloc) {
;             __builtin_amdgcn_fence(__ATOMIC_RELEASE, "agent");
;             asm volatile("s_waitcnt vmcnt(0)" ::: "memory");
;             const unsigned og = xb_add(&bar[XB_TOP], 1u);
;             const unsigned tg = og / nx;
;             if (og + 1u == (tg + 1u) * nx) xb_add(&bar[XB_TOPGEN], 1u);
;             else XB_SPIN(xb_ld(&bar[XB_TOPGEN]) == tg, bar);
;             __builtin_amdgcn_fence(__ATOMIC_ACQUIRE, "agent");
;             xb_add(&bar[XB_XGEN(b.x)], 1u);
;             asm volatile("s_waitcnt vmcnt(0)" ::: "memory");
;         } else {
;             XB_SPIN(xb_ld(&bar[XB_XGEN(b.x)]) == gen, bar);
.LBB0_819:
	s_mov_b64 s[6:7], exec
	v_readlane_b32 s3, v254, 21
	s_lshl_b32 s3, s3, 8
	v_mbcnt_lo_u32_b32 v0, s6, 0
	s_add_u32 s4, s28, s3
	v_mbcnt_hi_u32_b32 v0, s7, v0
	s_addc_u32 s5, s29, 0
	v_cmp_eq_u32_e32 vcc, 0, v0
	s_and_saveexec_b64 s[8:9], vcc
	s_cbranch_execz .LBB0_821
	s_bcnt1_i32_b64 s3, s[6:7]
	v_mov_b32_e32 v1, 0x1000
	v_mov_b32_e32 v2, s3
	global_atomic_add v1, v1, v2, s[4:5] offset:1024 sc0
	buffer_inv sc1
.LBB0_821:
	s_or_b64 exec, exec, s[8:9]
	v_cvt_f32_u32_e32 v2, v9
	s_waitcnt vmcnt(1)
	v_readfirstlane_b32 s3, v1
	v_sub_u32_e32 v1, 0, v9
	v_rcp_iflag_f32_e32 v2, v2
	v_add_u32_e32 v3, s3, v0
	v_mul_f32_e32 v2, 0x4f7ffffe, v2
	v_cvt_u32_f32_e32 v2, v2
	v_mul_lo_u32 v0, v1, v2
	v_mul_hi_u32 v0, v2, v0
	v_add_u32_e32 v0, v2, v0
	v_mul_hi_u32 v0, v3, v0
	v_mul_lo_u32 v1, v0, v9
	v_sub_u32_e32 v1, v3, v1
	v_add_u32_e32 v2, 1, v0
	v_cmp_ge_u32_e32 vcc, v1, v9
	s_nop 1
	v_cndmask_b32_e32 v0, v0, v2, vcc
	v_sub_u32_e32 v2, v1, v9
	v_cndmask_b32_e32 v1, v1, v2, vcc
	v_add_u32_e32 v2, 1, v0
	v_cmp_ge_u32_e32 vcc, v1, v9
	v_add_u32_e32 v1, 1, v3
	s_nop 0
	v_cndmask_b32_e32 v0, v0, v2, vcc
	v_mul_lo_u32 v2, v9, v0
	v_add_u32_e32 v2, v2, v9
	v_cmp_ne_u32_e32 vcc, v1, v2
	s_and_saveexec_b64 s[6:7], vcc
	s_xor_b64 s[6:7], exec, s[6:7]
	s_cbranch_execz .LBB0_835
	v_mov_b32_e32 v1, 0x3100
	global_load_dword v1, v1, s[28:29] offset:1024 sc1
	s_add_u32 s10, s28, 0x3500
	s_addc_u32 s11, s29, 0
	s_waitcnt vmcnt(0)
	v_cmp_eq_u32_e32 vcc, v1, v0
	s_and_saveexec_b64 s[8:9], vcc
	s_cbranch_execz .LBB0_834
	s_mov_b32 s3, 1
	s_mov_b64 s[12:13], 0
	v_mov_b32_e32 v1, 0
	s_branch .LBB0_825

; __device__ __forceinline__ unsigned xb_ld(unsigned* p)              { return __hip_atomic_load(p, __ATOMIC_RELAXED, __HIP_MEMORY_SCOPE_AGENT); }
; __device__ __forceinline__ unsigned xb_add(unsigned* p, unsigned v) { return __hip_atomic_fetch_add(p, v, __ATOMIC_RELAXED, __HIP_MEMORY_SCOPE_AGENT); }
; #define XB_SPIN(cond, bar) do { unsigned _sp = 0; while (cond) { __builtin_amdgcn_s_sleep(1); \
;     if ((++_sp & 255u) == 0u) { if (xb_ld(&(bar)[XB_TMO])) break; if (_sp > XB_SPIN_CAP) { atomicAdd(&(bar)[XB_TMO], 1u); break; } } } } while (0)
; __device__ __forceinline__ void xcc_barrier(unsigned* bar, unsigned* cnt, unsigned nloc, const bool xb_leader) {
;     ...
;         __builtin_amdgcn_s_waitcnt(0);
;         const unsigned old = xb_add(cnt, 1u), target = (old / nloc + 1u) * nloc;
;         XB_SPIN(xb_ld(cnt) < target, bar);
.LBB0_1549:
	s_or_b64 exec, exec, s[10:11]
	v_mov_b32_e32 v0, 0
	global_load_dword v3, v0, s[4:5] sc1
	buffer_inv sc1
	s_ashr_i32 s3, s33, 31
	s_lshr_b32 s3, s3, 29
	s_add_i32 s3, s33, s3
	s_ashr_i32 s6, s3, 3
	v_cvt_f32_u32_e32 v4, s6
	s_sub_i32 s3, 0, s6
	s_waitcnt vmcnt(2)
	v_readfirstlane_b32 s7, v2
	v_rcp_iflag_f32_e32 v4, v4
	s_nop 0
	v_add_u32_e32 v1, s7, v1
	v_mul_f32_e32 v4, 0x4f7ffffe, v4
	v_cvt_u32_f32_e32 v4, v4
	v_mul_lo_u32 v2, s3, v4
	v_mul_hi_u32 v2, v4, v2
	v_add_u32_e32 v2, v4, v2
	v_mul_hi_u32 v2, v1, v2
	v_mul_lo_u32 v4, v2, s6
	v_sub_u32_e32 v1, v1, v4
	v_add_u32_e32 v4, 1, v2
	v_cmp_le_u32_e32 vcc, s6, v1
	s_mov_b32 s3, 1
	s_nop 0
	v_cndmask_b32_e32 v2, v2, v4, vcc
	v_subrev_u32_e32 v4, s6, v1
	v_cndmask_b32_e32 v1, v1, v4, vcc
	v_add_u32_e32 v4, 1, v2
	v_cmp_le_u32_e32 vcc, s6, v1
	s_nop 1
	v_cndmask_b32_e32 v1, v2, v4, vcc
	v_mul_lo_u32 v1, s6, v1
	v_add_u32_e32 v1, s6, v1
	s_waitcnt vmcnt(1)
	v_cmp_lt_u32_e32 vcc, v3, v1
	s_and_saveexec_b64 s[6:7], vcc
	s_cbranch_execz .LBB0_1561
	s_mov_b64 s[10:11], 0
	s_branch .LBB0_1552

; __device__ __forceinline__ unsigned xb_ld(unsigned* p)              { return __hip_atomic_load(p, __ATOMIC_RELAXED, __HIP_MEMORY_SCOPE_AGENT); }
; __device__ __forceinline__ unsigned xb_add(unsigned* p, unsigned v) { return __hip_atomic_fetch_add(p, v, __ATOMIC_RELAXED, __HIP_MEMORY_SCOPE_AGENT); }
; #define XB_SPIN(cond, bar) do { unsigned _sp = 0; while (cond) { __builtin_amdgcn_s_sleep(1); \
;     if ((++_sp & 255u) == 0u) { if (xb_ld(&(bar)[XB_TMO])) break; if (_sp > XB_SPIN_CAP) { atomicAdd(&(bar)[XB_TMO], 1u); break; } } } } while (0)
; __device__ __forceinline__ void xcd_barrier(const XcdBarrier& b, const bool xb_leader) {
;     ...
;         const unsigned old = xb_add(&bar[XB_XSUB(b.x)], 1u);
;         const unsigned gen = old / nloc;
;         if (old + 1u == (gen + 1u) * nloc) {
;             __builtin_amdgcn_fence(__ATOMIC_RELEASE, "agent");
;             asm volatile("s_waitcnt vmcnt(0)" ::: "memory");
;             const unsigned og = xb_add(&bar[XB_TOP], 1u);
;             const unsigned tg = og / nx;
;             if (og + 1u == (tg + 1u) * nx) xb_add(&bar[XB_TOPGEN], 1u);
;             else XB_SPIN(xb_ld(&bar[XB_TOPGEN]) == tg, bar);
;             __builtin_amdgcn_fence(__ATOMIC_ACQUIRE, "agent");
;             xb_add(&bar[XB_XGEN(b.x)], 1u);
;             asm volatile("s_waitcnt vmcnt(0)" ::: "memory");
;         } else {
;             XB_SPIN(xb_ld(&bar[XB_XGEN(b.x)]) == gen, bar);
.LBB0_1590:
	s_mov_b64 s[6:7], exec
	v_readlane_b32 s3, v254, 21
	s_lshl_b32 s3, s3, 8
	v_mbcnt_lo_u32_b32 v0, s6, 0
	s_add_u32 s4, s28, s3
	v_mbcnt_hi_u32_b32 v0, s7, v0
	s_addc_u32 s5, s29, 0
	v_cmp_eq_u32_e32 vcc, 0, v0
	s_and_saveexec_b64 s[10:11], vcc
	s_cbranch_execz .LBB0_1592
	s_bcnt1_i32_b64 s3, s[6:7]
	v_mov_b32_e32 v1, 0x1000
	v_mov_b32_e32 v2, s3
	global_atomic_add v1, v1, v2, s[4:5] offset:1024 sc0
	buffer_inv sc1
.LBB0_1592:
	s_or_b64 exec, exec, s[10:11]
	v_cvt_f32_u32_e32 v2, v9
	s_waitcnt vmcnt(1)
	v_readfirstlane_b32 s3, v1
	v_sub_u32_e32 v1, 0, v9
	v_rcp_iflag_f32_e32 v2, v2
	v_add_u32_e32 v3, s3, v0
	v_mul_f32_e32 v2, 0x4f7ffffe, v2
	v_cvt_u32_f32_e32 v2, v2
	v_mul_lo_u32 v0, v1, v2
	v_mul_hi_u32 v0, v2, v0
	v_add_u32_e32 v0, v2, v0
	v_mul_hi_u32 v0, v3, v0
	v_mul_lo_u32 v1, v0, v9
	v_sub_u32_e32 v1, v3, v1
	v_add_u32_e32 v2, 1, v0
	v_cmp_ge_u32_e32 vcc, v1, v9
	s_nop 1
	v_cndmask_b32_e32 v0, v0, v2, vcc
	v_sub_u32_e32 v2, v1, v9
	v_cndmask_b32_e32 v1, v1, v2, vcc
	v_add_u32_e32 v2, 1, v0
	v_cmp_ge_u32_e32 vcc, v1, v9
	v_add_u32_e32 v1, 1, v3
	s_nop 0
	v_cndmask_b32_e32 v0, v0, v2, vcc
	v_mul_lo_u32 v2, v9, v0
	v_add_u32_e32 v2, v2, v9
	v_cmp_ne_u32_e32 vcc, v1, v2
	s_and_saveexec_b64 s[6:7], vcc
	s_xor_b64 s[6:7], exec, s[6:7]
	s_cbranch_execz .LBB0_1606
	v_mov_b32_e32 v1, 0x3100
	global_load_dword v1, v1, s[28:29] offset:1024 sc1
	s_add_u32 s12, s28, 0x3500
	s_addc_u32 s13, s29, 0
	s_waitcnt vmcnt(0)
	v_cmp_eq_u32_e32 vcc, v1, v0
	s_and_saveexec_b64 s[10:11], vcc
	s_cbranch_execz .LBB0_1605
	s_mov_b32 s3, 1
	s_mov_b64 s[14:15], 0
	v_mov_b32_e32 v1, 0
	s_branch .LBB0_1596

; __device__ __forceinline__ unsigned xb_ld(unsigned* p)              { return __hip_atomic_load(p, __ATOMIC_RELAXED, __HIP_MEMORY_SCOPE_AGENT); }
; __device__ __forceinline__ unsigned xb_add(unsigned* p, unsigned v) { return __hip_atomic_fetch_add(p, v, __ATOMIC_RELAXED, __HIP_MEMORY_SCOPE_AGENT); }
; #define XB_SPIN(cond, bar) do { unsigned _sp = 0; while (cond) { __builtin_amdgcn_s_sleep(1); \
;     if ((++_sp & 255u) == 0u) { if (xb_ld(&(bar)[XB_TMO])) break; if (_sp > XB_SPIN_CAP) { atomicAdd(&(bar)[XB_TMO], 1u); break; } } } } while (0)
; __device__ __forceinline__ void xcd_barrier(const XcdBarrier& b, const bool xb_leader) {
;     ...
;         const unsigned old = xb_add(&bar[XB_XSUB(b.x)], 1u);
;         const unsigned gen = old / nloc;
;         if (old + 1u == (gen + 1u) * nloc) {
;             __builtin_amdgcn_fence(__ATOMIC_RELEASE, "agent");
;             asm volatile("s_waitcnt vmcnt(0)" ::: "memory");
;             const unsigned og = xb_add(&bar[XB_TOP], 1u);
;             const unsigned tg = og / nx;
;             if (og + 1u == (tg + 1u) * nx) xb_add(&bar[XB_TOPGEN], 1u);
;             else XB_SPIN(xb_ld(&bar[XB_TOPGEN]) == tg, bar);
;             __builtin_amdgcn_fence(__ATOMIC_ACQUIRE, "agent");
;             xb_add(&bar[XB_XGEN(b.x)], 1u);
;             asm volatile("s_waitcnt vmcnt(0)" ::: "memory");
;         } else {
;             XB_SPIN(xb_ld(&bar[XB_XGEN(b.x)]) == gen, bar);
.LBB0_1906:
	s_mov_b64 s[2:3], exec
	v_readlane_b32 s0, v254, 21
	s_lshl_b32 s0, s0, 8
	v_mbcnt_lo_u32_b32 v0, s2, 0
	s_add_u32 s0, s28, s0
	v_mbcnt_hi_u32_b32 v0, s3, v0
	s_addc_u32 s1, s29, 0
	v_cmp_eq_u32_e32 vcc, 0, v0
	s_and_saveexec_b64 s[8:9], vcc
	s_cbranch_execz .LBB0_1908
	s_bcnt1_i32_b64 s2, s[2:3]
	v_mov_b32_e32 v1, 0x1000
	v_mov_b32_e32 v2, s2
	global_atomic_add v1, v1, v2, s[0:1] offset:1024 sc0
	buffer_inv sc1
.LBB0_1908:
	s_or_b64 exec, exec, s[8:9]
	v_cvt_f32_u32_e32 v2, v9
	s_waitcnt vmcnt(1)
	v_readfirstlane_b32 s2, v1
	v_sub_u32_e32 v1, 0, v9
	v_rcp_iflag_f32_e32 v2, v2
	v_add_u32_e32 v3, s2, v0
	v_mul_f32_e32 v2, 0x4f7ffffe, v2
	v_cvt_u32_f32_e32 v2, v2
	v_mul_lo_u32 v0, v1, v2
	v_mul_hi_u32 v0, v2, v0
	v_add_u32_e32 v0, v2, v0
	v_mul_hi_u32 v0, v3, v0
	v_mul_lo_u32 v1, v0, v9
	v_sub_u32_e32 v1, v3, v1
	v_add_u32_e32 v2, 1, v0
	v_cmp_ge_u32_e32 vcc, v1, v9
	s_nop 1
	v_cndmask_b32_e32 v0, v0, v2, vcc
	v_sub_u32_e32 v2, v1, v9
	v_cndmask_b32_e32 v1, v1, v2, vcc
	v_add_u32_e32 v2, 1, v0
	v_cmp_ge_u32_e32 vcc, v1, v9
	v_add_u32_e32 v1, 1, v3
	s_nop 0
	v_cndmask_b32_e32 v0, v0, v2, vcc
	v_mul_lo_u32 v2, v9, v0
	v_add_u32_e32 v2, v2, v9
	v_cmp_ne_u32_e32 vcc, v1, v2
	s_and_saveexec_b64 s[2:3], vcc
	s_xor_b64 s[2:3], exec, s[2:3]
	s_cbranch_execz .LBB0_1922
	v_mov_b32_e32 v1, 0x3100
	global_load_dword v1, v1, s[28:29] offset:1024 sc1
	s_add_u32 s12, s28, 0x3500
	s_addc_u32 s13, s29, 0
	s_waitcnt vmcnt(0)
	v_cmp_eq_u32_e32 vcc, v1, v0
	s_and_saveexec_b64 s[8:9], vcc
	s_cbranch_execz .LBB0_1921
	s_mov_b32 s26, 1
	s_mov_b64 s[14:15], 0
	v_mov_b32_e32 v1, 0
	s_branch .LBB0_1912
